# ring-16 hybrid with 4KiB load bursts instead of 8KiB
# speedup vs baseline: 1.0185x; 1.0185x over previous
.Lk1_contm_3:
	global_load_dwordx4 v[28:31], v1, s[6:7] nt
	s_add_u32 s6, s6, 0x400
	s_addc_u32 s7, s7, 0
	global_load_dwordx4 v[32:35], v1, s[6:7] nt
	s_add_u32 s6, s6, 0x400
	s_addc_u32 s7, s7, 0
	global_load_dwordx4 v[36:39], v1, s[6:7] nt
	s_add_u32 s6, s6, 0x400
	s_addc_u32 s7, s7, 0
	global_load_dwordx4 v[40:43], v1, s[6:7] nt
	s_add_u32 s6, s6, 0x400
	s_addc_u32 s7, s7, 0
	s_waitcnt vmcnt(15)
	v_or3_b32 v12, v44, v45, v46
	v_or_b32_e32 v12, v12, v47
	v_cmp_ne_u32_e32 vcc, 0, v12
	s_cbranch_vccnz .Lk1_hitm_4
.Lk1_contm_4:
	s_waitcnt vmcnt(14)
	v_or3_b32 v12, v48, v49, v50
	v_or_b32_e32 v12, v12, v51
	v_cmp_ne_u32_e32 vcc, 0, v12
	s_cbranch_vccnz .Lk1_hitm_5
.Lk1_contm_5:
	s_waitcnt vmcnt(13)
	v_or3_b32 v12, v52, v53, v54
	v_or_b32_e32 v12, v12, v55
	v_cmp_ne_u32_e32 vcc, 0, v12
	s_cbranch_vccnz .Lk1_hitm_6
.Lk1_contm_6:
	s_waitcnt vmcnt(12)
	v_or3_b32 v12, v56, v57, v58
	v_or_b32_e32 v12, v12, v59
	v_cmp_ne_u32_e32 vcc, 0, v12
	s_cbranch_vccnz .Lk1_hitm_7
.Lk1_contm_7:
	global_load_dwordx4 v[44:47], v1, s[6:7] nt
	s_add_u32 s6, s6, 0x400
	s_addc_u32 s7, s7, 0
	global_load_dwordx4 v[48:51], v1, s[6:7] nt
	s_add_u32 s6, s6, 0x400
	s_addc_u32 s7, s7, 0
	global_load_dwordx4 v[52:55], v1, s[6:7] nt
	s_add_u32 s6, s6, 0x400
	s_addc_u32 s7, s7, 0
	global_load_dwordx4 v[56:59], v1, s[6:7] nt
	s_add_u32 s6, s6, 0x400
	s_addc_u32 s7, s7, 0
	s_waitcnt vmcnt(15)
	v_or3_b32 v12, v60, v61, v62
	v_or_b32_e32 v12, v12, v63
	v_cmp_ne_u32_e32 vcc, 0, v12
	s_cbranch_vccnz .Lk1_hitm_8

.Lk1_contm_11:
	global_load_dwordx4 v[60:63], v1, s[6:7] nt
	s_add_u32 s6, s6, 0x400
	s_addc_u32 s7, s7, 0
	global_load_dwordx4 v[64:67], v1, s[6:7] nt
	s_add_u32 s6, s6, 0x400
	s_addc_u32 s7, s7, 0
	global_load_dwordx4 v[68:71], v1, s[6:7] nt
	s_add_u32 s6, s6, 0x400
	s_addc_u32 s7, s7, 0
	global_load_dwordx4 v[72:75], v1, s[6:7] nt
	s_add_u32 s6, s6, 0x400
	s_addc_u32 s7, s7, 0
	s_waitcnt vmcnt(15)
	v_or3_b32 v12, v76, v77, v78
	v_or_b32_e32 v12, v12, v79
	v_cmp_ne_u32_e32 vcc, 0, v12
	s_cbranch_vccnz .Lk1_hitm_12
.Lk1_contm_12:
	s_waitcnt vmcnt(14)
	v_or3_b32 v12, v80, v81, v82
	v_or_b32_e32 v12, v12, v83
	v_cmp_ne_u32_e32 vcc, 0, v12
	s_cbranch_vccnz .Lk1_hitm_13
.Lk1_contm_13:
	s_waitcnt vmcnt(13)
	v_or3_b32 v12, v84, v85, v86
	v_or_b32_e32 v12, v12, v87
	v_cmp_ne_u32_e32 vcc, 0, v12
	s_cbranch_vccnz .Lk1_hitm_14
.Lk1_contm_14:
	s_waitcnt vmcnt(12)
	v_or3_b32 v12, v88, v89, v90
	v_or_b32_e32 v12, v12, v91
	v_cmp_ne_u32_e32 vcc, 0, v12
	s_cbranch_vccnz .Lk1_hitm_15
.Lk1_contm_15:
	global_load_dwordx4 v[76:79], v1, s[6:7] nt
	s_add_u32 s6, s6, 0x400
	s_addc_u32 s7, s7, 0
	global_load_dwordx4 v[80:83], v1, s[6:7] nt
	s_add_u32 s6, s6, 0x400
	s_addc_u32 s7, s7, 0
	global_load_dwordx4 v[84:87], v1, s[6:7] nt
	s_add_u32 s6, s6, 0x400
	s_addc_u32 s7, s7, 0
	global_load_dwordx4 v[88:91], v1, s[6:7] nt
	s_add_u32 s6, s6, 0x400
	s_addc_u32 s7, s7, 0
	s_mov_b32 s18, s58
	s_add_u32 s60, s26, 2
	s_cmp_lt_u32 s60, 14
	s_cbranch_scc0 .Lk1_dynid
	s_add_u32 s57, s59, s60
	s_branch .Lk1_haveid
